# speedup vs baseline: 1.0000x; 1.0000x over previous
_Z6gat_k2PKDF16_S0_S0_PKfPf:
	s_load_dwordx8 s[4:11], s[0:1], 0x0
	s_load_dwordx2 s[12:13], s[0:1], 0x20
	v_readfirstlane_b32 s14, v0
	v_and_b32_e32 v46, 63, v0
	v_lshlrev_b32_e32 v1, 4, v46
	s_and_b32 s16, s2, 1
	s_bfe_u32 s17, s2, 0x60003
	s_lshr_b32 s18, s2, 1
	s_lshr_b32 s15, s14, 6
	s_lshl_b32 s19, s16, 19
	s_lshl_b32 s23, s15, 16
	s_add_u32 s19, s19, s23
	s_lshl_b32 s23, s15, 11
	v_add_u32_e32 v47, s23, v1
	v_and_b32_e32 v44, 31, v0
	v_lshlrev_b32_e32 v45, 2, v44
	s_lshl_b32 s23, s18, 8
	v_add_u32_e32 v45, s23, v45
	s_waitcnt lgkmcnt(0)
	global_load_dword v42, v45, s[10:11]
	global_load_dword v43, v45, s[10:11] offset:128
	global_load_dwordx4 v[48:51], v47, s[6:7]
	global_load_dwordx4 v[52:55], v47, s[6:7] offset:1024
	global_load_dwordx4 v[56:59], v47, s[8:9]
	global_load_dwordx4 v[60:63], v47, s[8:9] offset:1024
	s_add_u32 s20, s4, s19
	s_addc_u32 s21, s5, 0
	s_add_u32 s23, s17, 0
	s_and_b32 s23, s23, 63
	s_lshl_b32 s23, s23, 10
	s_add_u32 s24, s20, s23
	s_addc_u32 s25, s21, 0
	global_load_dwordx4 v[64:67], v1, s[24:25]
	s_add_u32 s23, s17, 1
	s_and_b32 s23, s23, 63
	s_lshl_b32 s23, s23, 10
	s_add_u32 s24, s20, s23
	s_addc_u32 s25, s21, 0
	global_load_dwordx4 v[68:71], v1, s[24:25]
	s_add_u32 s23, s17, 2
	s_and_b32 s23, s23, 63
	s_lshl_b32 s23, s23, 10
	s_add_u32 s24, s20, s23
	s_addc_u32 s25, s21, 0
	global_load_dwordx4 v[72:75], v1, s[24:25]
	s_add_u32 s23, s17, 3
	s_and_b32 s23, s23, 63
	s_lshl_b32 s23, s23, 10
	s_add_u32 s24, s20, s23
	s_addc_u32 s25, s21, 0
	global_load_dwordx4 v[76:79], v1, s[24:25]
	s_add_u32 s23, s17, 4
	s_and_b32 s23, s23, 63
	s_lshl_b32 s23, s23, 10
	s_add_u32 s24, s20, s23
	s_addc_u32 s25, s21, 0
	global_load_dwordx4 v[80:83], v1, s[24:25]
	s_add_u32 s23, s17, 5
	s_and_b32 s23, s23, 63
	s_lshl_b32 s23, s23, 10
	s_add_u32 s24, s20, s23
	s_addc_u32 s25, s21, 0
	global_load_dwordx4 v[84:87], v1, s[24:25]
	s_add_u32 s23, s17, 6
	s_and_b32 s23, s23, 63
	s_lshl_b32 s23, s23, 10
	s_add_u32 s24, s20, s23
	s_addc_u32 s25, s21, 0
	global_load_dwordx4 v[88:91], v1, s[24:25]
	s_add_u32 s23, s17, 7
	s_and_b32 s23, s23, 63
	s_lshl_b32 s23, s23, 10
	s_add_u32 s24, s20, s23
	s_addc_u32 s25, s21, 0
	global_load_dwordx4 v[92:95], v1, s[24:25]
	v_accvgpr_write_b32 a0, 0
	v_accvgpr_write_b32 a1, 0
	v_accvgpr_write_b32 a2, 0
	v_accvgpr_write_b32 a3, 0
	v_accvgpr_write_b32 a4, 0
	v_accvgpr_write_b32 a5, 0
	v_accvgpr_write_b32 a6, 0
	v_accvgpr_write_b32 a7, 0
	v_accvgpr_write_b32 a8, 0
	v_accvgpr_write_b32 a9, 0
	v_accvgpr_write_b32 a10, 0
	v_accvgpr_write_b32 a11, 0
	v_accvgpr_write_b32 a12, 0
	v_accvgpr_write_b32 a13, 0
	v_accvgpr_write_b32 a14, 0
	v_accvgpr_write_b32 a15, 0
	v_accvgpr_write_b32 a16, 0
	v_accvgpr_write_b32 a17, 0
	v_accvgpr_write_b32 a18, 0
	v_accvgpr_write_b32 a19, 0
	v_accvgpr_write_b32 a20, 0
	v_accvgpr_write_b32 a21, 0
	v_accvgpr_write_b32 a22, 0
	v_accvgpr_write_b32 a23, 0
	v_accvgpr_write_b32 a24, 0
	v_accvgpr_write_b32 a25, 0
	v_accvgpr_write_b32 a26, 0
	v_accvgpr_write_b32 a27, 0
	v_accvgpr_write_b32 a28, 0
	v_accvgpr_write_b32 a29, 0
	v_accvgpr_write_b32 a30, 0
	v_accvgpr_write_b32 a31, 0
	v_accvgpr_write_b32 a32, 0
	v_accvgpr_write_b32 a33, 0
	v_accvgpr_write_b32 a34, 0
	v_accvgpr_write_b32 a35, 0
	v_accvgpr_write_b32 a36, 0
	v_accvgpr_write_b32 a37, 0
	v_accvgpr_write_b32 a38, 0
	v_accvgpr_write_b32 a39, 0
	v_mov_b32_e32 v2, 0
	v_mov_b32_e32 v3, 0
	v_mov_b32_e32 v4, 0
	v_mov_b32_e32 v5, 0
	v_lshrrev_b32_e32 v44, 1, v46
	v_subrev_u32_e32 v44, s17, v44
	v_and_b32_e32 v44, 63, v44
	v_lshlrev_b32_e32 v44, 5, v44
	v_and_b32_e32 v45, 1, v46
	v_lshl_or_b32 v44, v45, 4, v44
	v_xor_b32_e32 v45, 0x400, v44
	s_mul_i32 s23, s15, 0x1900
	s_add_u32 s23, s23, 0x11000
	v_add_u32_e32 v44, s23, v44
	v_add_u32_e32 v45, s23, v45
	v_add_u32_e32 v47, s23, v1
	ds_write_b128 v47, v[2:5] offset:4096
	ds_write_b128 v47, v[2:5] offset:5120
	s_waitcnt vmcnt(8)
	ds_write_b128 v44, v[48:51]
	ds_write_b128 v45, v[52:55]
	ds_write_b128 v44, v[56:59] offset:2048
	ds_write_b128 v45, v[60:63] offset:2048
	v_cvt_f16_f32_e32 v42, v42
	v_cvt_f16_f32_e32 v43, v43
	s_mov_b32 s28, 0x5040100
	v_perm_b32 v42, v42, v42, s28
	v_perm_b32 v43, v43, v43, s28
	v_lshrrev_b32_e32 v44, 5, v46
	v_and_b32_e32 v45, 15, v46
	v_bfe_u32 v47, v46, 4, 1
	v_cmp_eq_u32_e32 vcc, v45, v47
	v_lshlrev_b32_e32 v44, 4, v44
	v_add_u32_e32 v46, s23, v44
	v_add_u32_e32 v45, 0x800, v46
	v_mov_b32_e32 v47, s23
	v_add_u32_e32 v47, 0x1000, v47
	v_cndmask_b32_e32 v47, v47, v45, vcc
	s_waitcnt lgkmcnt(0)
	ds_read_b128 v[144:147], v46
	ds_read_b128 v[148:151], v46 offset:32
	ds_read_b128 v[160:163], v47
	ds_read_b128 v[152:155], v46 offset:64
	ds_read_b128 v[164:167], v47 offset:32
	s_add_u32 s27, s17, 8
	s_lshl_b32 s27, s27, 10
	s_add_u32 s29, s17, 63
	s_lshl_b32 s29, s29, 10
	s_movk_i32 s28, 0x400
	s_mov_b32 s26, 0
	s_waitcnt lgkmcnt(4)
	v_pk_max_u16 v128, v144, v42
	v_pk_max_u16 v129, v145, v42
	v_pk_max_u16 v130, v146, v42
	v_pk_max_u16 v131, v147, v42
	v_pk_max_u16 v136, v144, v43
	v_pk_max_u16 v137, v145, v43
	v_pk_max_u16 v138, v146, v43
	v_pk_max_u16 v139, v147, v43
	s_mov_b32 s31, 0xfc00
.Lk2_loop:
	s_and_b32 s23, s27, s31
	s_add_u32 s24, s20, s23
	s_addc_u32 s25, s21, 0
	s_add_u32 s27, s27, s28
	s_waitcnt vmcnt(7)
	s_waitcnt lgkmcnt(2)
	v_mfma_f32_32x32x16_f16 a[0:15], v[64:67], v[128:131], a[0:15]
	v_pk_max_u16 v132, v148, v42
	v_pk_max_u16 v133, v149, v42
	v_pk_max_u16 v134, v150, v42
	v_pk_max_u16 v135, v151, v42
	v_mfma_f32_32x32x16_f16 a[16:31], v[64:67], v[136:139], a[16:31]
	v_pk_max_u16 v140, v148, v43
	v_pk_max_u16 v141, v149, v43
	v_pk_max_u16 v142, v150, v43
	v_pk_max_u16 v143, v151, v43
	v_mfma_f32_16x16x32_f16 a[32:35], v[160:163], v[128:131], a[32:35]
	global_load_dwordx4 v[64:67], v1, s[24:25]
	ds_read_b128 v[156:159], v46 offset:96
	ds_read_b128 v[168:171], v47 offset:64
	v_mfma_f32_16x16x32_f16 a[36:39], v[160:163], v[136:139], a[36:39]
	s_and_b32 s23, s27, s31
	s_add_u32 s24, s20, s23
	s_addc_u32 s25, s21, 0
	s_add_u32 s27, s27, s28
	s_waitcnt vmcnt(7)
	s_waitcnt lgkmcnt(2)
	v_mfma_f32_32x32x16_f16 a[0:15], v[68:71], v[132:135], a[0:15]
	v_pk_max_u16 v128, v152, v42
	v_pk_max_u16 v129, v153, v42
	v_pk_max_u16 v130, v154, v42
	v_pk_max_u16 v131, v155, v42
	v_mfma_f32_32x32x16_f16 a[16:31], v[68:71], v[140:143], a[16:31]
	v_pk_max_u16 v136, v152, v43
	v_pk_max_u16 v137, v153, v43
	v_pk_max_u16 v138, v154, v43
	v_pk_max_u16 v139, v155, v43
	v_mfma_f32_16x16x32_f16 a[32:35], v[164:167], v[132:135], a[32:35]
	global_load_dwordx4 v[68:71], v1, s[24:25]
	ds_read_b128 v[144:147], v46 offset:128
	ds_read_b128 v[172:175], v47 offset:96
	v_mfma_f32_16x16x32_f16 a[36:39], v[164:167], v[140:143], a[36:39]
	s_and_b32 s23, s27, s31
	s_add_u32 s24, s20, s23
	s_addc_u32 s25, s21, 0
	s_add_u32 s27, s27, s28
	s_waitcnt vmcnt(7)
	s_waitcnt lgkmcnt(2)
	v_mfma_f32_32x32x16_f16 a[0:15], v[72:75], v[128:131], a[0:15]
	v_pk_max_u16 v132, v156, v42
	v_pk_max_u16 v133, v157, v42
	v_pk_max_u16 v134, v158, v42
	v_pk_max_u16 v135, v159, v42
	v_mfma_f32_32x32x16_f16 a[16:31], v[72:75], v[136:139], a[16:31]
	v_pk_max_u16 v140, v156, v43
	v_pk_max_u16 v141, v157, v43
	v_pk_max_u16 v142, v158, v43
	v_pk_max_u16 v143, v159, v43
	v_mfma_f32_16x16x32_f16 a[32:35], v[168:171], v[128:131], a[32:35]
	global_load_dwordx4 v[72:75], v1, s[24:25]
	ds_read_b128 v[148:151], v46 offset:160
	ds_read_b128 v[160:163], v47 offset:128
	v_mfma_f32_16x16x32_f16 a[36:39], v[168:171], v[136:139], a[36:39]
	s_and_b32 s23, s27, s31
	s_add_u32 s24, s20, s23
	s_addc_u32 s25, s21, 0
	s_add_u32 s27, s27, s28
	s_waitcnt vmcnt(7)
	s_waitcnt lgkmcnt(2)
	v_mfma_f32_32x32x16_f16 a[0:15], v[76:79], v[132:135], a[0:15]
	v_pk_max_u16 v128, v144, v42
	v_pk_max_u16 v129, v145, v42
	v_pk_max_u16 v130, v146, v42
	v_pk_max_u16 v131, v147, v42
	v_mfma_f32_32x32x16_f16 a[16:31], v[76:79], v[140:143], a[16:31]
	v_pk_max_u16 v136, v144, v43
	v_pk_max_u16 v137, v145, v43
	v_pk_max_u16 v138, v146, v43
	v_pk_max_u16 v139, v147, v43
	v_mfma_f32_16x16x32_f16 a[32:35], v[172:175], v[132:135], a[32:35]
	global_load_dwordx4 v[76:79], v1, s[24:25]
	ds_read_b128 v[152:155], v46 offset:192
	ds_read_b128 v[164:167], v47 offset:160
	v_mfma_f32_16x16x32_f16 a[36:39], v[172:175], v[140:143], a[36:39]
	s_and_b32 s23, s27, s31
	s_add_u32 s24, s20, s23
	s_addc_u32 s25, s21, 0
	s_add_u32 s27, s27, s28
	s_waitcnt vmcnt(7)
	s_waitcnt lgkmcnt(2)
	v_mfma_f32_32x32x16_f16 a[0:15], v[80:83], v[128:131], a[0:15]
	v_pk_max_u16 v132, v148, v42
	v_pk_max_u16 v133, v149, v42
	v_pk_max_u16 v134, v150, v42
	v_pk_max_u16 v135, v151, v42
	v_mfma_f32_32x32x16_f16 a[16:31], v[80:83], v[136:139], a[16:31]
	v_pk_max_u16 v140, v148, v43
	v_pk_max_u16 v141, v149, v43
	v_pk_max_u16 v142, v150, v43
	v_pk_max_u16 v143, v151, v43
	v_mfma_f32_16x16x32_f16 a[32:35], v[160:163], v[128:131], a[32:35]
	global_load_dwordx4 v[80:83], v1, s[24:25]
	ds_read_b128 v[156:159], v46 offset:224
	ds_read_b128 v[168:171], v47 offset:192
	v_mfma_f32_16x16x32_f16 a[36:39], v[160:163], v[136:139], a[36:39]
	s_and_b32 s23, s27, s31
	s_add_u32 s24, s20, s23
	s_addc_u32 s25, s21, 0
	s_add_u32 s27, s27, s28
	s_waitcnt vmcnt(7)
	s_waitcnt lgkmcnt(2)
	v_mfma_f32_32x32x16_f16 a[0:15], v[84:87], v[132:135], a[0:15]
	v_pk_max_u16 v128, v152, v42
	v_pk_max_u16 v129, v153, v42
	v_pk_max_u16 v130, v154, v42
	v_pk_max_u16 v131, v155, v42
	v_mfma_f32_32x32x16_f16 a[16:31], v[84:87], v[140:143], a[16:31]
	v_pk_max_u16 v136, v152, v43
	v_pk_max_u16 v137, v153, v43
	v_pk_max_u16 v138, v154, v43
	v_pk_max_u16 v139, v155, v43
	v_mfma_f32_16x16x32_f16 a[32:35], v[164:167], v[132:135], a[32:35]
	global_load_dwordx4 v[84:87], v1, s[24:25]
	ds_read_b128 v[144:147], v46 offset:256
	ds_read_b128 v[172:175], v47 offset:224
	v_mfma_f32_16x16x32_f16 a[36:39], v[164:167], v[140:143], a[36:39]
	s_and_b32 s23, s27, s31
	s_add_u32 s24, s20, s23
	s_addc_u32 s25, s21, 0
	s_add_u32 s27, s27, s28
	s_waitcnt vmcnt(7)
	s_waitcnt lgkmcnt(2)
	v_mfma_f32_32x32x16_f16 a[0:15], v[88:91], v[128:131], a[0:15]
	v_pk_max_u16 v132, v156, v42
	v_pk_max_u16 v133, v157, v42
	v_pk_max_u16 v134, v158, v42
	v_pk_max_u16 v135, v159, v42
	v_mfma_f32_32x32x16_f16 a[16:31], v[88:91], v[136:139], a[16:31]
	v_pk_max_u16 v140, v156, v43
	v_pk_max_u16 v141, v157, v43
	v_pk_max_u16 v142, v158, v43
	v_pk_max_u16 v143, v159, v43
	v_mfma_f32_16x16x32_f16 a[32:35], v[168:171], v[128:131], a[32:35]
	global_load_dwordx4 v[88:91], v1, s[24:25]
	ds_read_b128 v[148:151], v46 offset:288
	ds_read_b128 v[160:163], v47 offset:256
	v_mfma_f32_16x16x32_f16 a[36:39], v[168:171], v[136:139], a[36:39]
	s_and_b32 s23, s27, s31
	s_add_u32 s24, s20, s23
	s_addc_u32 s25, s21, 0
	s_add_u32 s27, s27, s28
	s_waitcnt vmcnt(7)
	s_waitcnt lgkmcnt(2)
	v_mfma_f32_32x32x16_f16 a[0:15], v[92:95], v[132:135], a[0:15]
	v_pk_max_u16 v128, v144, v42
	v_pk_max_u16 v129, v145, v42
	v_pk_max_u16 v130, v146, v42
	v_pk_max_u16 v131, v147, v42
	v_mfma_f32_32x32x16_f16 a[16:31], v[92:95], v[140:143], a[16:31]
	v_pk_max_u16 v136, v144, v43
	v_pk_max_u16 v137, v145, v43
	v_pk_max_u16 v138, v146, v43
	v_pk_max_u16 v139, v147, v43
	v_mfma_f32_16x16x32_f16 a[32:35], v[172:175], v[132:135], a[32:35]
	global_load_dwordx4 v[92:95], v1, s[24:25]
	ds_read_b128 v[152:155], v46 offset:320
	ds_read_b128 v[164:167], v47 offset:288
	v_mfma_f32_16x16x32_f16 a[36:39], v[172:175], v[140:143], a[36:39]
	s_add_u32 s26, s26, 1
	v_add_u32_e32 v46, 256, v46
	v_add_u32_e32 v47, 256, v47
	s_cmp_eq_u32 s26, 7
	s_cselect_b32 s27, s29, s27
	s_cselect_b32 s28, 0, s28
	s_cmp_lt_u32 s26, 8
	s_cbranch_scc1 .Lk2_loop
	v_and_b32_e32 v2, 63, v0
	v_lshrrev_b32_e32 v3, 5, v2
	v_and_b32_e32 v4, 31, v0
	s_lshl_b32 s23, s15, 4
	v_add_u32_e32 v3, s23, v3
	v_mul_u32_u24_e32 v3, 0x210, v3
	v_lshl_add_u32 v3, v4, 4, v3
	v_cmp_gt_u32_e32 vcc, 16, v2
	ds_write_b128 v3, a[0:3]
	ds_write_b128 v3, a[16:19] offset:4224
	ds_write_b128 v3, a[4:7] offset:1056
	ds_write_b128 v3, a[20:23] offset:5280
	ds_write_b128 v3, a[8:11] offset:2112
	ds_write_b128 v3, a[24:27] offset:6336
	ds_write_b128 v3, a[12:15] offset:3168
	ds_write_b128 v3, a[28:31] offset:7392
	s_and_saveexec_b64 s[2:3], vcc
	s_cbranch_execz .Lk2_nodred
	v_lshlrev_b32_e32 v5, 2, v2
	s_lshl_b32 s23, s15, 8
	v_add_u32_e32 v5, s23, v5
	v_add_u32_e32 v5, 0x10800, v5
	ds_write2_b32 v5, a32, a33 offset1:16
	ds_write2_b32 v5, a36, a37 offset0:32 offset1:48
.Lk2_nodred:
	s_or_b64 exec, exec, s[2:3]
	v_lshrrev_b32_e32 v6, 3, v0
	v_and_b32_e32 v7, 7, v0
	v_lshrrev_b32_e32 v8, 8, v0
	v_bfe_u32 v9, v0, 3, 5
	v_lshlrev_b32_e32 v10, 2, v9
	v_lshl_or_b32 v10, v8, 7, v10
	v_add_u32_e32 v10, 0x10800, v10
	v_mul_u32_u24_e32 v11, 0x1080, v8
	v_mul_u32_u24_e32 v12, 0x210, v7
	v_lshlrev_b32_e32 v13, 4, v9
	v_add3_u32 v11, v11, v12, v13
	s_lshl_b32 s4, s18, 6
	v_or_b32_e32 v14, s4, v6
	v_mov_b32_e32 v15, 0
	v_lshlrev_b64 v[16:17], 8, v[14:15]
	v_lshl_add_u64 v[16:17], s[12:13], 0, v[16:17]
	s_lshl_b32 s2, s16, 7
	s_mov_b32 s3, 0
	v_lshl_add_u64 v[16:17], v[16:17], 0, s[2:3]
	v_lshlrev_b32_e32 v14, 4, v7
	v_lshl_add_u64 v[16:17], v[16:17], 0, v[14:15]
	s_waitcnt lgkmcnt(0)
	s_barrier
	ds_read_b128 v[18:21], v11
	ds_read_b128 v[22:25], v11 offset:8448
	ds_read_b128 v[26:29], v11 offset:16896
	ds_read_b128 v[30:33], v11 offset:25344
	ds_read_b128 v[34:37], v11 offset:33792
	ds_read_b128 v[38:41], v11 offset:42240
	ds_read_b128 v[42:45], v11 offset:50688
	ds_read_b128 v[46:49], v11 offset:59136
	ds_read_b32 v50, v10
	ds_read_b32 v51, v10 offset:256
	ds_read_b32 v52, v10 offset:512
	ds_read_b32 v53, v10 offset:768
	ds_read_b32 v54, v10 offset:1024
	ds_read_b32 v55, v10 offset:1280
	ds_read_b32 v56, v10 offset:1536
	s_waitcnt lgkmcnt(13)
	ds_read_b32 v57, v10 offset:1792
	v_pk_add_f32 v[60:61], v[20:21], v[24:25]
	v_pk_add_f32 v[58:59], v[18:19], v[22:23]
	s_waitcnt lgkmcnt(13)
	v_pk_add_f32 v[60:61], v[60:61], v[28:29]
	v_pk_add_f32 v[58:59], v[58:59], v[26:27]
	s_waitcnt lgkmcnt(12)
	v_pk_add_f32 v[60:61], v[60:61], v[32:33]
	v_pk_add_f32 v[58:59], v[58:59], v[30:31]
	s_waitcnt lgkmcnt(11)
	v_pk_add_f32 v[60:61], v[60:61], v[36:37]
	v_pk_add_f32 v[58:59], v[58:59], v[34:35]
	s_waitcnt lgkmcnt(10)
	v_pk_add_f32 v[60:61], v[60:61], v[40:41]
	v_pk_add_f32 v[58:59], v[58:59], v[38:39]
	s_waitcnt lgkmcnt(9)
	v_pk_add_f32 v[60:61], v[60:61], v[44:45]
	v_pk_add_f32 v[58:59], v[58:59], v[42:43]
	s_waitcnt lgkmcnt(8)
	v_pk_add_f32 v[60:61], v[60:61], v[48:49]
	v_pk_add_f32 v[58:59], v[58:59], v[46:47]
	s_waitcnt lgkmcnt(6)
	v_add_f32_e32 v2, v50, v51
	s_waitcnt lgkmcnt(5)
	v_add_f32_e32 v2, v2, v52
	s_waitcnt lgkmcnt(4)
	v_add_f32_e32 v2, v2, v53
	s_waitcnt lgkmcnt(3)
	v_add_f32_e32 v2, v2, v54
	s_waitcnt lgkmcnt(2)
	v_add_f32_e32 v2, v2, v55
	s_waitcnt lgkmcnt(1)
	v_add_f32_e32 v2, v2, v56
	s_waitcnt lgkmcnt(0)
	v_add_f32_e32 v2, v2, v57
	v_div_scale_f32 v3, s[2:3], v2, v2, 1.0
	v_rcp_f32_e32 v4, v3
	v_div_scale_f32 v5, vcc, 1.0, v2, 1.0
	v_fma_f32 v6, -v3, v4, 1.0
	v_fmac_f32_e32 v4, v6, v4
	v_mul_f32_e32 v6, v5, v4
	v_fma_f32 v7, -v3, v6, v5
	v_fmac_f32_e32 v6, v7, v4
	v_fma_f32 v3, -v3, v6, v5
	v_div_fmas_f32 v3, v3, v4, v6
	v_div_fixup_f32 v8, v3, v2, 1.0
	v_pk_mul_f32 v[60:61], v[60:61], v[8:9] op_sel_hi:[1,0]
	v_pk_mul_f32 v[58:59], v[58:59], v[8:9] op_sel_hi:[1,0]
	global_store_dwordx4 v[16:17], v[58:61], off
	s_endpgm

	.amdhsa_kernel _Z6gat_k2PKDF16_S0_S0_PKfPf
		.amdhsa_group_segment_fixed_size 120832
		.amdhsa_private_segment_fixed_size 0
		.amdhsa_kernarg_size 40
		.amdhsa_user_sgpr_count 2
		.amdhsa_user_sgpr_dispatch_ptr 0
		.amdhsa_user_sgpr_queue_ptr 0
		.amdhsa_user_sgpr_kernarg_segment_ptr 1
		.amdhsa_user_sgpr_dispatch_id 0
		.amdhsa_user_sgpr_kernarg_preload_length 0
		.amdhsa_user_sgpr_kernarg_preload_offset 0
		.amdhsa_user_sgpr_private_segment_size 0
		.amdhsa_uses_dynamic_stack 0
		.amdhsa_enable_private_segment 0
		.amdhsa_system_sgpr_workgroup_id_x 1
		.amdhsa_system_sgpr_workgroup_id_y 0
		.amdhsa_system_sgpr_workgroup_id_z 0
		.amdhsa_system_sgpr_workgroup_info 0
		.amdhsa_system_vgpr_workitem_id 0
		.amdhsa_next_free_vgpr 216
		.amdhsa_next_free_sgpr 96
		.amdhsa_accum_offset 176
		.amdhsa_reserve_vcc 1
		.amdhsa_float_round_mode_32 0
		.amdhsa_float_round_mode_16_64 0
		.amdhsa_float_denorm_mode_32 3
		.amdhsa_float_denorm_mode_16_64 3
		.amdhsa_dx10_clamp 1
		.amdhsa_ieee_mode 1
		.amdhsa_fp16_overflow 0
		.amdhsa_tg_split 0
		.amdhsa_exception_fp_ieee_invalid_op 0
		.amdhsa_exception_fp_denorm_src 0
		.amdhsa_exception_fp_ieee_div_zero 0
		.amdhsa_exception_fp_ieee_overflow 0
		.amdhsa_exception_fp_ieee_underflow 0
		.amdhsa_exception_fp_ieee_inexact 0
		.amdhsa_exception_int_div_zero 0
	.end_amdhsa_kernel

amdhsa.kernels:
  - .agpr_count:     32
    .args:
      - .actual_access:  read_only
        .address_space:  global
        .offset:         0
        .size:           8
        .value_kind:     global_buffer
      - .actual_access:  read_only
        .address_space:  global
        .offset:         8
        .size:           8
        .value_kind:     global_buffer
      - .actual_access:  read_only
        .address_space:  global
        .offset:         16
        .size:           8
        .value_kind:     global_buffer
      - .actual_access:  read_only
        .address_space:  global
        .offset:         24
        .size:           8
        .value_kind:     global_buffer
      - .actual_access:  write_only
        .address_space:  global
        .offset:         32
        .size:           8
        .value_kind:     global_buffer
      - .actual_access:  write_only
        .address_space:  global
        .offset:         40
        .size:           8
        .value_kind:     global_buffer
      - .actual_access:  write_only
        .address_space:  global
        .offset:         48
        .size:           8
        .value_kind:     global_buffer
      - .actual_access:  write_only
        .address_space:  global
        .offset:         56
        .size:           8
        .value_kind:     global_buffer
    .group_segment_fixed_size: 68352
    .kernarg_segment_align: 8
    .kernarg_segment_size: 64
    .language:       OpenCL C
    .language_version:
      - 2
      - 0
    .max_flat_workgroup_size: 256
    .name:           _Z6gat_k1PKfS0_S0_S0_PDF16_S1_S1_Pf
    .private_segment_fixed_size: 0
    .sgpr_count:     18
    .sgpr_spill_count: 0
    .symbol:         _Z6gat_k1PKfS0_S0_S0_PDF16_S1_S1_Pf.kd
    .uniform_work_group_size: 1
    .uses_dynamic_stack: false
    .vgpr_count:     156
    .vgpr_spill_count: 0
    .wavefront_size: 64
  - .agpr_count:     40
    .args:
      - .actual_access:  read_only
        .address_space:  global
        .offset:         0
        .size:           8
        .value_kind:     global_buffer
      - .actual_access:  read_only
        .address_space:  global
        .offset:         8
        .size:           8
        .value_kind:     global_buffer
      - .actual_access:  read_only
        .address_space:  global
        .offset:         16
        .size:           8
        .value_kind:     global_buffer
      - .actual_access:  read_only
        .address_space:  global
        .offset:         24
        .size:           8
        .value_kind:     global_buffer
      - .actual_access:  write_only
        .address_space:  global
        .offset:         32
        .size:           8
        .value_kind:     global_buffer
    .group_segment_fixed_size: 120832
    .kernarg_segment_align: 8
    .kernarg_segment_size: 40
    .language:       OpenCL C
    .language_version:
      - 2
      - 0
    .max_flat_workgroup_size: 512
    .name:           _Z6gat_k2PKDF16_S0_S0_PKfPf
    .private_segment_fixed_size: 0
    .sgpr_count:     24
    .sgpr_spill_count: 0
    .symbol:         _Z6gat_k2PKDF16_S0_S0_PKfPf.kd
    .uniform_work_group_size: 1
    .uses_dynamic_stack: false
    .vgpr_count:     216
    .vgpr_spill_count: 0
    .wavefront_size: 64
